# same as previous with a grid-size guard: expert 8-9 conversion moves to the in-projection tail only when the grid has 256 workgroups
# baseline (speedup 1.0000x reference)
.LBB0_5:
	s_or_b64 exec, exec, s[0:1]
	s_cmp_lt_i32 s82, 1
	s_cselect_b64 s[0:1], -1, 0
	s_cmp_gt_i32 s83, 0
	s_cselect_b64 s[4:5], -1, 0
	s_and_b64 s[16:17], s[0:1], s[4:5]
	s_andn2_b64 vcc, exec, s[16:17]
	s_cbranch_vccnz .LBB0_231
	s_lshl_b32 s26, s2, 3
	s_cmpk_eq_u32 s3, 0x100
	s_cselect_b32 s0, 0x300, 0
	s_add_i32 s2, s2, s0
	s_cmpk_gt_i32 s2, 0x6df
	s_mov_b64 s[10:11], s[86:87]
	s_barrier
	s_cbranch_scc1 .LBB0_168
	s_add_u32 s27, s80, 0x1d00000
	s_addc_u32 s28, s81, 0
	s_add_u32 s29, s80, 0x1100000
	s_addc_u32 s30, s81, 0
	s_add_u32 s31, s80, 0x1500000
	s_addc_u32 s33, s81, 0
	s_and_b32 s18, s2, 1
	s_cmp_eq_u32 s18, 0
	s_cselect_b64 s[0:1], -1, 0
	s_add_u32 s35, s80, 0x1000000
	s_addc_u32 s36, s81, 0
	s_add_u32 s37, s80, 0x2500000
	s_addc_u32 s38, s81, 0
	s_add_u32 s39, s80, 0x74700000
	s_addc_u32 s40, s81, 0
	s_add_u32 s41, s80, 0x24e00000
	s_addc_u32 s42, s81, 0
	s_add_u32 s43, s80, 0x4e00000
	s_addc_u32 s44, s81, 0
	v_lshlrev_b32_e32 v1, 2, v253
	v_lshrrev_b32_e32 v2, 2, v253
	v_or_b32_e32 v3, 0x200, v253
	v_or_b32_e32 v4, 0x400, v253
	v_or_b32_e32 v66, 0x600, v253
	v_lshrrev_b32_e32 v130, 4, v253
	v_or_b32_e32 v5, 0xa00, v253
	s_cmpk_gt_i32 s2, 0x2ff
	v_or_b32_e32 v6, 0xe00, v253
	s_cbranch_scc0 .LBB0_13
	s_cmpk_gt_u32 s2, 0x58f
	s_cbranch_scc0 .LBB0_14
	s_lshl_b32 s4, s2, 4
	s_and_b32 s12, s4, 0x7f80
	s_cmpk_gt_u32 s2, 0x59f
	s_cbranch_scc0 .LBB0_15
	s_lshl_b32 s5, s2, 8
	s_and_b32 s13, s5, 0x700
	s_lshl_b32 s14, s13, 11
	s_cmpk_gt_u32 s2, 0x61f
	s_cbranch_scc0 .LBB0_17
	s_cmpk_gt_u32 s2, 0x65f
	s_cbranch_scc0 .LBB0_18
	s_and_b32 s4, s4, 0x7fffff80
	s_addk_i32 s4, 0x9a00
	s_mov_b32 s5, 0
	s_lshl_b64 s[6:7], s[4:5], 13
	s_load_dwordx2 s[8:9], s[10:11], 0xc8
	s_add_u32 s5, s27, s14
	s_addc_u32 s15, s28, 0
	s_add_u32 s4, s5, s4
	s_addc_u32 s5, s15, 0
	s_waitcnt lgkmcnt(0)
	s_add_u32 s6, s8, s6
	s_addc_u32 s7, s9, s7
	s_lshl_b32 s8, s13, 2
	s_add_u32 s8, s6, s8
	s_addc_u32 s9, s7, 0
	s_mov_b64 s[6:7], 0
	s_branch .LBB0_19

.LBB0_168:
	s_cmpk_eq_u32 s3, 0x100
	s_cselect_b32 s0, 0x300, 0
	s_sub_i32 s2, s2, s0
	v_lshl_or_b32 v2, s2, 9, v253
	s_movk_i32 s0, 0x2900
	v_cmp_gt_i32_e32 vcc, s0, v2
	s_and_saveexec_b64 s[0:1], vcc
	s_cbranch_execz .LBB0_187
	s_lshl_b32 s4, s3, 9
	v_ashrrev_i32_e32 v3, 31, v2
	v_lshl_add_u64 v[4:5], v[2:3], 2, s[80:81]
	s_mov_b64 s[6:7], 0xa00000
	s_ashr_i32 s5, s4, 31
	v_lshl_add_u64 v[4:5], v[4:5], 0, s[6:7]
	s_lshl_b64 s[6:7], s[4:5], 2
	s_mov_b64 s[8:9], 0
	s_movk_i32 s5, 0x7ff
	s_movk_i32 s22, 0xbff
	s_movk_i32 s23, 0x1bff
	s_movk_i32 s24, 0x1c0f
	s_movk_i32 s25, 0x1cff
	v_mov_b32_e32 v7, 0
	s_movk_i32 s27, 0x28ff
	s_branch .LBB0_171

.LBB0_479:
	s_cmpk_lg_u32 s3, 0x100
	s_cbranch_scc1 .Lp2t_skip
	s_cmpk_lt_u32 s2, 0x88
	s_cbranch_scc1 .Lp2t_skip
	s_mov_b64 s[28:29], s[4:5]
	s_lshr_b32 s33, s92, 6
	v_mbcnt_lo_u32_b32 v65, -1, 0
	v_mbcnt_hi_u32_b32 v65, -1, v65
	s_mov_b64 s[16:17], s[86:87]
	s_mov_b64 s[18:19], s[80:81]
	s_mov_b32 s8, s33
	s_sub_i32 s0, s2, 0x88
	s_lshl_b32 s0, s0, 3
	s_add_i32 s20, s8, s0
	s_cmpk_gt_i32 s20, 0x17ff
	s_cbranch_scc1 .Lp2t_end
	s_add_i32 s0, s20, 0x11000
	s_add_i32 s14, s20, 0x4000
	s_cmpk_lt_i32 s20, 0x1000
	s_cselect_b32 s9, s14, s0
	s_cmp_gt_i32 s9, 0xffff
	s_cbranch_scc0 .Lp2t_1227
	s_load_dwordx2 s[0:1], s[16:17], 0x110
	s_add_i32 s4, s9, 0xffff0000
	s_mov_b32 s7, 0
	s_lshr_b32 s6, s4, 10
	s_lshl_b64 s[4:5], s[6:7], 24
	s_waitcnt lgkmcnt(0)
	s_add_u32 s0, s0, s4
	s_addc_u32 s1, s1, s5
	s_lshl_b32 s4, s9, 1
	s_and_b32 s10, s4, 0x780
	s_lshl_b32 s4, s10, 13
	s_add_u32 s0, s0, s4
	s_addc_u32 s1, s1, 0
	s_lshl_b32 s4, s9, 5
	s_and_b32 s11, s4, 0x7e0
	s_lshl_b32 s4, s11, 2
	s_add_u32 s4, s0, s4
	s_addc_u32 s5, s1, 0
	s_lshl_b64 s[0:1], s[6:7], 22
	s_lshl_b32 s6, s11, 11
	s_add_u32 s0, s18, s0
	s_addc_u32 s1, s19, s1
	s_add_u32 s0, s0, s6
	s_addc_u32 s1, s1, 0
	s_add_u32 s0, s0, s10
	s_addc_u32 s1, s1, 0
	s_add_u32 s0, s0, 0x24e00000
	s_addc_u32 s1, s1, 0
	s_mov_b32 s21, 0x42800000
	s_cbranch_execz .Lp2t_1228
	s_branch .Lp2t_1229
